# gate/up epilogue: adjacent scalar f32 mul/add pairs of the silu chain issued as v_pk_mul_f32 / v_pk_add_f32 (same f32 arithmetic); on top of the previous stack
# speedup vs baseline: 1.0001x; 1.0001x over previous
; __device__ __forceinline__ unsigned cvt_pk_bf16(float lo, float hi) { f32x2_c v = {lo, hi}; bf16x2_c b = __builtin_convertvector(v, bf16x2_c); return __builtin_bit_cast(unsigned, b); }
; __device__ __forceinline__ float silu_f(float g) { return g * __builtin_amdgcn_rcpf(1.0f + __builtin_amdgcn_exp2f(-1.44269504f * g)); }
;     __device__ __forceinline__ void operator()(const f32x4 (&acc)[2][2][4][2], const Unit& u, int wr, int wc, int fr, int fq) const {
;     ...
;         for (int ai = 0; ai < 2; ++ai)
; #pragma unroll
;             for (int m = 0; m < 4; ++m) { bf16_t* rowp = O + (size_t)(row0 + ai * HALF + m * 16) * ldc + col0;
;                 const float rs = my[(ai * 4 + m) * 16];
;                 const f32x4 a0 = acc[ai][0][m][0] * rs, a1 = acc[ai][0][m][1] * rs, g0 = acc[ai][1][m][0] * rs, g1 = acc[ai][1][m][1] * rs;
;                 u32x4 w; w.x = cvt_pk_bf16(a0[0] * silu_f(g0[0]), a0[1] * silu_f(g0[1])); w.y = cvt_pk_bf16(a0[2] * silu_f(g0[2]), a0[3] * silu_f(g0[3]));
;                 w.z = cvt_pk_bf16(a1[0] * silu_f(g1[0]), a1[1] * silu_f(g1[1])); w.w = cvt_pk_bf16(a1[2] * silu_f(g1[2]), a1[3] * silu_f(g1[3]));
;                 *(u32x4*)rowp = w; }
.LBB0_153:
	s_mov_b32 s72, 0xbfb8aa3b
	s_mov_b32 s73, 0xbfb8aa3b
	s_waitcnt lgkmcnt(0)
	v_mov_b64_e32 v[142:143], s[94:95]
	s_movk_i32 s4, 0x2c00
	v_lshl_or_b32 v158, s2, 7, v162
	v_mad_u64_u32 v[164:165], s[2:3], v144, s4, v[142:143]
	v_mov_b32_e32 v144, v165
	v_ashrrev_i32_e32 v159, 31, v158
	v_mad_u64_u32 v[144:145], s[2:3], v145, s4, v[144:145]
	v_mov_b32_e32 v165, v144
	v_lshlrev_b64 v[144:145], 1, v[158:159]
	v_lshl_add_u64 v[158:159], v[164:165], 0, v[144:145]
	ds_read2_b32 v[164:165], v161 offset1:16
	s_and_b64 vcc, exec, s[8:9]
	s_waitcnt lgkmcnt(0)
	v_pk_mul_f32 v[166:167], v[118:119], v[164:165] op_sel_hi:[1,0]
	v_pk_mul_f32 v[118:119], v[116:117], v[164:165] op_sel_hi:[1,0]
	v_pk_mul_f32 v[116:117], v[128:129], v[164:165] op_sel_hi:[1,0]
	v_pk_mul_f32 v[120:121], v[120:121], v[164:165] op_sel_hi:[1,0]
	v_pk_mul_f32 v[128:129], v[116:117], s[72:73]
	v_exp_f32_e32 v128, v128
	v_exp_f32_e32 v129, v129
	v_pk_mul_f32 v[130:131], v[130:131], v[164:165] op_sel_hi:[1,0]
	v_pk_mul_f32 v[122:123], v[122:123], v[164:165] op_sel_hi:[1,0]
	v_pk_add_f32 v[128:129], v[128:129], 1.0 op_sel_hi:[1,0]
	v_rcp_f32_e32 v128, v128
	v_rcp_f32_e32 v129, v129
	v_pk_mul_f32 v[124:125], v[124:125], v[164:165] op_sel_hi:[1,0]
	v_pk_mul_f32 v[126:127], v[126:127], v[164:165] op_sel_hi:[1,0]
	v_pk_mul_f32 v[116:117], v[116:117], v[128:129]
	s_nop 0
	v_pk_mul_f32 v[116:117], v[120:121], v[116:117]
	s_nop 0
	v_cvt_pk_bf16_f32 v116, v116, v117
	v_mul_f32_e32 v117, 0xbfb8aa3b, v130
	v_exp_f32_e32 v117, v117
	s_nop 0
	v_add_f32_e32 v117, 1.0, v117
	v_rcp_f32_e32 v120, v117
	v_mul_f32_e32 v117, 0xbfb8aa3b, v131
	v_exp_f32_e32 v117, v117
	s_nop 0
	v_add_f32_e32 v117, 1.0, v117
	v_rcp_f32_e32 v121, v117
	s_nop 0
	v_pk_mul_f32 v[120:121], v[130:131], v[120:121]
	s_nop 0
	v_pk_mul_f32 v[120:121], v[122:123], v[120:121]
	s_nop 0
	v_cvt_pk_bf16_f32 v117, v120, v121
	v_pk_mul_f32 v[120:121], v[124:125], s[72:73]
	v_exp_f32_e32 v120, v120
	v_exp_f32_e32 v121, v121
	s_nop 0
	v_pk_add_f32 v[120:121], v[120:121], 1.0 op_sel_hi:[1,0]
	v_rcp_f32_e32 v120, v120
	v_rcp_f32_e32 v121, v121
	s_nop 0
	v_pk_mul_f32 v[120:121], v[124:125], v[120:121]
	s_nop 0
	v_pk_mul_f32 v[118:119], v[118:119], v[120:121]
	s_nop 0
	v_cvt_pk_bf16_f32 v118, v118, v119
	v_mul_f32_e32 v119, 0xbfb8aa3b, v126
	v_exp_f32_e32 v119, v119
	s_nop 0
	v_add_f32_e32 v119, 1.0, v119
	v_rcp_f32_e32 v120, v119
	v_mul_f32_e32 v119, 0xbfb8aa3b, v127
	v_exp_f32_e32 v119, v119
	s_nop 0
	v_add_f32_e32 v119, 1.0, v119
	v_rcp_f32_e32 v121, v119
	s_nop 0
	v_pk_mul_f32 v[120:121], v[126:127], v[120:121]
	s_nop 0
	v_pk_mul_f32 v[120:121], v[166:167], v[120:121]
	s_nop 0
	v_cvt_pk_bf16_f32 v119, v120, v121
	global_store_dwordx4 v[158:159], v[116:119], off
	s_nop 1
	v_mad_u64_u32 v[116:117], s[2:3], v156, s4, v[142:143]
	v_mov_b32_e32 v118, v117
	v_mad_u64_u32 v[118:119], s[2:3], v157, s4, v[118:119]
	v_mov_b32_e32 v117, v118
	v_mov_b32_e32 v118, v165
	v_pk_mul_f32 v[120:121], v[102:103], v[118:119] op_sel_hi:[1,0]
	v_pk_mul_f32 v[102:103], v[100:101], v[118:119] op_sel_hi:[1,0]
	v_pk_mul_f32 v[100:101], v[112:113], v[118:119] op_sel_hi:[1,0]
	v_pk_mul_f32 v[104:105], v[104:105], v[118:119] op_sel_hi:[1,0]
	v_pk_mul_f32 v[112:113], v[100:101], s[72:73]
	v_exp_f32_e32 v112, v112
	v_exp_f32_e32 v113, v113
	v_pk_mul_f32 v[114:115], v[114:115], v[118:119] op_sel_hi:[1,0]
	v_pk_mul_f32 v[106:107], v[106:107], v[118:119] op_sel_hi:[1,0]
	v_pk_add_f32 v[112:113], v[112:113], 1.0 op_sel_hi:[1,0]
	v_rcp_f32_e32 v112, v112
	v_rcp_f32_e32 v113, v113
	v_pk_mul_f32 v[108:109], v[108:109], v[118:119] op_sel_hi:[1,0]
	v_pk_mul_f32 v[110:111], v[110:111], v[118:119] op_sel_hi:[1,0]
	v_lshl_add_u64 v[116:117], v[116:117], 0, v[144:145]
	v_pk_mul_f32 v[100:101], v[100:101], v[112:113]
	s_nop 0
	v_pk_mul_f32 v[100:101], v[104:105], v[100:101]
	s_nop 0
	v_cvt_pk_bf16_f32 v100, v100, v101
	v_mul_f32_e32 v101, 0xbfb8aa3b, v114
	v_exp_f32_e32 v101, v101
	s_nop 0
	v_add_f32_e32 v101, 1.0, v101
	v_rcp_f32_e32 v104, v101
	v_mul_f32_e32 v101, 0xbfb8aa3b, v115
	v_exp_f32_e32 v101, v101
	s_nop 0
	v_add_f32_e32 v101, 1.0, v101
	v_rcp_f32_e32 v105, v101
	s_nop 0
	v_pk_mul_f32 v[104:105], v[114:115], v[104:105]
	s_nop 0
	v_pk_mul_f32 v[104:105], v[106:107], v[104:105]
	s_nop 0
	v_cvt_pk_bf16_f32 v101, v104, v105
	v_pk_mul_f32 v[104:105], v[108:109], s[72:73]
	v_exp_f32_e32 v104, v104
	v_exp_f32_e32 v105, v105
	s_nop 0
	v_pk_add_f32 v[104:105], v[104:105], 1.0 op_sel_hi:[1,0]
	v_rcp_f32_e32 v104, v104
	v_rcp_f32_e32 v105, v105
	s_nop 0
	v_pk_mul_f32 v[104:105], v[108:109], v[104:105]
	s_nop 0
	v_pk_mul_f32 v[102:103], v[102:103], v[104:105]
	s_nop 0
	v_cvt_pk_bf16_f32 v102, v102, v103
	v_mul_f32_e32 v103, 0xbfb8aa3b, v110
	v_exp_f32_e32 v103, v103
	s_nop 0
	v_add_f32_e32 v103, 1.0, v103
	v_rcp_f32_e32 v104, v103
	v_mul_f32_e32 v103, 0xbfb8aa3b, v111
	v_exp_f32_e32 v103, v103
	s_nop 0
	v_add_f32_e32 v103, 1.0, v103
	v_rcp_f32_e32 v105, v103
	s_nop 0
	v_pk_mul_f32 v[104:105], v[110:111], v[104:105]
	s_nop 0
	v_pk_mul_f32 v[104:105], v[120:121], v[104:105]
	s_nop 0
	v_cvt_pk_bf16_f32 v103, v104, v105
	global_store_dwordx4 v[116:117], v[100:103], off
	s_nop 1
	v_mad_u64_u32 v[100:101], s[2:3], v154, s4, v[142:143]
	v_mov_b32_e32 v102, v101
	v_mad_u64_u32 v[102:103], s[2:3], v155, s4, v[102:103]
	v_mov_b32_e32 v101, v102
	ds_read2_b32 v[102:103], v161 offset0:32 offset1:48
	v_lshl_add_u64 v[100:101], v[100:101], 0, v[144:145]
	s_waitcnt lgkmcnt(0)
; __device__ __forceinline__ unsigned cvt_pk_bf16(float lo, float hi) { f32x2_c v = {lo, hi}; bf16x2_c b = __builtin_convertvector(v, bf16x2_c); return __builtin_bit_cast(unsigned, b); }
; __device__ __forceinline__ float silu_f(float g) { return g * __builtin_amdgcn_rcpf(1.0f + __builtin_amdgcn_exp2f(-1.44269504f * g)); }
;     __device__ __forceinline__ void operator()(const f32x4 (&acc)[2][2][4][2], const Unit& u, int wr, int wc, int fr, int fq) const {
;     ...
;         for (int ai = 0; ai < 2; ++ai)
; #pragma unroll
;             for (int m = 0; m < 4; ++m) { bf16_t* rowp = O + (size_t)(row0 + ai * HALF + m * 16) * ldc + col0;
;                 const float rs = my[(ai * 4 + m) * 16];
;                 const f32x4 a0 = acc[ai][0][m][0] * rs, a1 = acc[ai][0][m][1] * rs, g0 = acc[ai][1][m][0] * rs, g1 = acc[ai][1][m][1] * rs;
;                 u32x4 w; w.x = cvt_pk_bf16(a0[0] * silu_f(g0[0]), a0[1] * silu_f(g0[1])); w.y = cvt_pk_bf16(a0[2] * silu_f(g0[2]), a0[3] * silu_f(g0[3]));
;                 w.z = cvt_pk_bf16(a1[0] * silu_f(g1[0]), a1[1] * silu_f(g1[1])); w.w = cvt_pk_bf16(a1[2] * silu_f(g1[2]), a1[3] * silu_f(g1[3]));
;                 *(u32x4*)rowp = w; }
	v_pk_mul_f32 v[104:105], v[86:87], v[102:103] op_sel_hi:[1,0]
	v_pk_mul_f32 v[86:87], v[84:85], v[102:103] op_sel_hi:[1,0]
	v_pk_mul_f32 v[84:85], v[96:97], v[102:103] op_sel_hi:[1,0]
	v_pk_mul_f32 v[88:89], v[88:89], v[102:103] op_sel_hi:[1,0]
	v_pk_mul_f32 v[96:97], v[84:85], s[72:73]
	v_exp_f32_e32 v96, v96
	v_exp_f32_e32 v97, v97
	v_pk_mul_f32 v[98:99], v[98:99], v[102:103] op_sel_hi:[1,0]
	v_pk_mul_f32 v[90:91], v[90:91], v[102:103] op_sel_hi:[1,0]
	v_pk_add_f32 v[96:97], v[96:97], 1.0 op_sel_hi:[1,0]
	v_rcp_f32_e32 v96, v96
	v_rcp_f32_e32 v97, v97
	v_pk_mul_f32 v[92:93], v[92:93], v[102:103] op_sel_hi:[1,0]
	v_pk_mul_f32 v[94:95], v[94:95], v[102:103] op_sel_hi:[1,0]
	v_pk_mul_f32 v[84:85], v[84:85], v[96:97]
	s_nop 0
	v_pk_mul_f32 v[84:85], v[88:89], v[84:85]
	s_nop 0
	v_cvt_pk_bf16_f32 v84, v84, v85
	v_mul_f32_e32 v85, 0xbfb8aa3b, v98
	v_exp_f32_e32 v85, v85
	s_nop 0
	v_add_f32_e32 v85, 1.0, v85
	v_rcp_f32_e32 v88, v85
	v_mul_f32_e32 v85, 0xbfb8aa3b, v99
	v_exp_f32_e32 v85, v85
	s_nop 0
	v_add_f32_e32 v85, 1.0, v85
	v_rcp_f32_e32 v89, v85
	s_nop 0
	v_pk_mul_f32 v[88:89], v[98:99], v[88:89]
	s_nop 0
	v_pk_mul_f32 v[88:89], v[90:91], v[88:89]
	s_nop 0
	v_cvt_pk_bf16_f32 v85, v88, v89
	v_pk_mul_f32 v[88:89], v[92:93], s[72:73]
	v_exp_f32_e32 v88, v88
	v_exp_f32_e32 v89, v89
	s_nop 0
	v_pk_add_f32 v[88:89], v[88:89], 1.0 op_sel_hi:[1,0]
	v_rcp_f32_e32 v88, v88
	v_rcp_f32_e32 v89, v89
	s_nop 0
	v_pk_mul_f32 v[88:89], v[92:93], v[88:89]
	s_nop 0
	v_pk_mul_f32 v[86:87], v[86:87], v[88:89]
	s_nop 0
	v_cvt_pk_bf16_f32 v86, v86, v87
	v_mul_f32_e32 v87, 0xbfb8aa3b, v94
	v_exp_f32_e32 v87, v87
	s_nop 0
	v_add_f32_e32 v87, 1.0, v87
	v_rcp_f32_e32 v88, v87
	v_mul_f32_e32 v87, 0xbfb8aa3b, v95
	v_exp_f32_e32 v87, v87
	s_nop 0
	v_add_f32_e32 v87, 1.0, v87
	v_rcp_f32_e32 v89, v87
	s_nop 0
	v_pk_mul_f32 v[88:89], v[94:95], v[88:89]
	s_nop 0
	v_pk_mul_f32 v[88:89], v[104:105], v[88:89]
	s_nop 0
	v_cvt_pk_bf16_f32 v87, v88, v89
	global_store_dwordx4 v[100:101], v[84:87], off
	s_nop 1
	v_mad_u64_u32 v[84:85], s[2:3], v152, s4, v[142:143]
	v_mov_b32_e32 v86, v85
	v_mad_u64_u32 v[86:87], s[2:3], v153, s4, v[86:87]
	v_mov_b32_e32 v85, v86
	v_mov_b32_e32 v86, v103
	v_pk_mul_f32 v[88:89], v[70:71], v[86:87] op_sel_hi:[1,0]
	v_pk_mul_f32 v[70:71], v[68:69], v[86:87] op_sel_hi:[1,0]
	v_pk_mul_f32 v[68:69], v[80:81], v[86:87] op_sel_hi:[1,0]
	v_pk_mul_f32 v[72:73], v[72:73], v[86:87] op_sel_hi:[1,0]
	v_pk_mul_f32 v[80:81], v[68:69], s[72:73]
	v_exp_f32_e32 v80, v80
	v_exp_f32_e32 v81, v81
	v_pk_mul_f32 v[82:83], v[82:83], v[86:87] op_sel_hi:[1,0]
	v_pk_mul_f32 v[74:75], v[74:75], v[86:87] op_sel_hi:[1,0]
	v_pk_add_f32 v[80:81], v[80:81], 1.0 op_sel_hi:[1,0]
	v_rcp_f32_e32 v80, v80
	v_rcp_f32_e32 v81, v81
	v_pk_mul_f32 v[76:77], v[76:77], v[86:87] op_sel_hi:[1,0]
	v_pk_mul_f32 v[78:79], v[78:79], v[86:87] op_sel_hi:[1,0]
	v_lshl_add_u64 v[84:85], v[84:85], 0, v[144:145]
	v_pk_mul_f32 v[68:69], v[68:69], v[80:81]
	s_nop 0
	v_pk_mul_f32 v[68:69], v[72:73], v[68:69]
	s_nop 0
	v_cvt_pk_bf16_f32 v68, v68, v69
	v_mul_f32_e32 v69, 0xbfb8aa3b, v82
	v_exp_f32_e32 v69, v69
	s_nop 0
	v_add_f32_e32 v69, 1.0, v69
	v_rcp_f32_e32 v72, v69
	v_mul_f32_e32 v69, 0xbfb8aa3b, v83
	v_exp_f32_e32 v69, v69
	s_nop 0
	v_add_f32_e32 v69, 1.0, v69
	v_rcp_f32_e32 v73, v69
	s_nop 0
	v_pk_mul_f32 v[72:73], v[82:83], v[72:73]
	s_nop 0
	v_pk_mul_f32 v[72:73], v[74:75], v[72:73]
	s_nop 0
	v_cvt_pk_bf16_f32 v69, v72, v73
	v_pk_mul_f32 v[72:73], v[76:77], s[72:73]
	v_exp_f32_e32 v72, v72
	v_exp_f32_e32 v73, v73
	s_nop 0
	v_pk_add_f32 v[72:73], v[72:73], 1.0 op_sel_hi:[1,0]
	v_rcp_f32_e32 v72, v72
	v_rcp_f32_e32 v73, v73
	s_nop 0
	v_pk_mul_f32 v[72:73], v[76:77], v[72:73]
	s_nop 0
	v_pk_mul_f32 v[70:71], v[70:71], v[72:73]
	s_nop 0
	v_cvt_pk_bf16_f32 v70, v70, v71
	v_mul_f32_e32 v71, 0xbfb8aa3b, v78
	v_exp_f32_e32 v71, v71
	s_nop 0
	v_add_f32_e32 v71, 1.0, v71
	v_rcp_f32_e32 v72, v71
	v_mul_f32_e32 v71, 0xbfb8aa3b, v79
	v_exp_f32_e32 v71, v71
	s_nop 0
	v_add_f32_e32 v71, 1.0, v71
	v_rcp_f32_e32 v73, v71
	s_nop 0
	v_pk_mul_f32 v[72:73], v[78:79], v[72:73]
	s_nop 0
	v_pk_mul_f32 v[72:73], v[88:89], v[72:73]
	s_nop 0
	v_cvt_pk_bf16_f32 v71, v72, v73
	global_store_dwordx4 v[84:85], v[68:71], off
	s_nop 1
	v_mad_u64_u32 v[68:69], s[2:3], v150, s4, v[142:143]
	v_mov_b32_e32 v70, v69
	v_mad_u64_u32 v[70:71], s[2:3], v151, s4, v[70:71]
	v_mov_b32_e32 v69, v70
	ds_read2_b32 v[70:71], v161 offset0:64 offset1:80
	v_lshl_add_u64 v[68:69], v[68:69], 0, v[144:145]
	s_waitcnt lgkmcnt(0)
; __device__ __forceinline__ unsigned cvt_pk_bf16(float lo, float hi) { f32x2_c v = {lo, hi}; bf16x2_c b = __builtin_convertvector(v, bf16x2_c); return __builtin_bit_cast(unsigned, b); }
; __device__ __forceinline__ float silu_f(float g) { return g * __builtin_amdgcn_rcpf(1.0f + __builtin_amdgcn_exp2f(-1.44269504f * g)); }
;     __device__ __forceinline__ void operator()(const f32x4 (&acc)[2][2][4][2], const Unit& u, int wr, int wc, int fr, int fq) const {
;     ...
;         for (int ai = 0; ai < 2; ++ai)
; #pragma unroll
;             for (int m = 0; m < 4; ++m) { bf16_t* rowp = O + (size_t)(row0 + ai * HALF + m * 16) * ldc + col0;
;                 const float rs = my[(ai * 4 + m) * 16];
;                 const f32x4 a0 = acc[ai][0][m][0] * rs, a1 = acc[ai][0][m][1] * rs, g0 = acc[ai][1][m][0] * rs, g1 = acc[ai][1][m][1] * rs;
;                 u32x4 w; w.x = cvt_pk_bf16(a0[0] * silu_f(g0[0]), a0[1] * silu_f(g0[1])); w.y = cvt_pk_bf16(a0[2] * silu_f(g0[2]), a0[3] * silu_f(g0[3]));
;                 w.z = cvt_pk_bf16(a1[0] * silu_f(g1[0]), a1[1] * silu_f(g1[1])); w.w = cvt_pk_bf16(a1[2] * silu_f(g1[2]), a1[3] * silu_f(g1[3]));
;                 *(u32x4*)rowp = w; }
	v_pk_mul_f32 v[72:73], v[54:55], v[70:71] op_sel_hi:[1,0]
	v_pk_mul_f32 v[54:55], v[52:53], v[70:71] op_sel_hi:[1,0]
	v_pk_mul_f32 v[52:53], v[64:65], v[70:71] op_sel_hi:[1,0]
	v_pk_mul_f32 v[56:57], v[56:57], v[70:71] op_sel_hi:[1,0]
	v_pk_mul_f32 v[64:65], v[52:53], s[72:73]
	v_exp_f32_e32 v64, v64
	v_exp_f32_e32 v65, v65
	v_pk_mul_f32 v[66:67], v[66:67], v[70:71] op_sel_hi:[1,0]
	v_pk_mul_f32 v[58:59], v[58:59], v[70:71] op_sel_hi:[1,0]
	v_pk_add_f32 v[64:65], v[64:65], 1.0 op_sel_hi:[1,0]
	v_rcp_f32_e32 v64, v64
	v_rcp_f32_e32 v65, v65
	v_pk_mul_f32 v[60:61], v[60:61], v[70:71] op_sel_hi:[1,0]
	v_pk_mul_f32 v[62:63], v[62:63], v[70:71] op_sel_hi:[1,0]
	v_pk_mul_f32 v[52:53], v[52:53], v[64:65]
	s_nop 0
	v_pk_mul_f32 v[52:53], v[56:57], v[52:53]
	s_nop 0
	v_cvt_pk_bf16_f32 v52, v52, v53
	v_mul_f32_e32 v53, 0xbfb8aa3b, v66
	v_exp_f32_e32 v53, v53
	s_nop 0
	v_add_f32_e32 v53, 1.0, v53
	v_rcp_f32_e32 v56, v53
	v_mul_f32_e32 v53, 0xbfb8aa3b, v67
	v_exp_f32_e32 v53, v53
	s_nop 0
	v_add_f32_e32 v53, 1.0, v53
	v_rcp_f32_e32 v57, v53
	s_nop 0
	v_pk_mul_f32 v[56:57], v[66:67], v[56:57]
	s_nop 0
	v_pk_mul_f32 v[56:57], v[58:59], v[56:57]
	s_nop 0
	v_cvt_pk_bf16_f32 v53, v56, v57
	v_pk_mul_f32 v[56:57], v[60:61], s[72:73]
	v_exp_f32_e32 v56, v56
	v_exp_f32_e32 v57, v57
	s_nop 0
	v_pk_add_f32 v[56:57], v[56:57], 1.0 op_sel_hi:[1,0]
	v_rcp_f32_e32 v56, v56
	v_rcp_f32_e32 v57, v57
	s_nop 0
	v_pk_mul_f32 v[56:57], v[60:61], v[56:57]
	s_nop 0
	v_pk_mul_f32 v[54:55], v[54:55], v[56:57]
	s_nop 0
	v_cvt_pk_bf16_f32 v54, v54, v55
	v_mul_f32_e32 v55, 0xbfb8aa3b, v62
	v_exp_f32_e32 v55, v55
	s_nop 0
	v_add_f32_e32 v55, 1.0, v55
	v_rcp_f32_e32 v56, v55
	v_mul_f32_e32 v55, 0xbfb8aa3b, v63
	v_exp_f32_e32 v55, v55
	s_nop 0
	v_add_f32_e32 v55, 1.0, v55
	v_rcp_f32_e32 v57, v55
	s_nop 0
	v_pk_mul_f32 v[56:57], v[62:63], v[56:57]
	s_nop 0
	v_pk_mul_f32 v[56:57], v[72:73], v[56:57]
	s_nop 0
	v_cvt_pk_bf16_f32 v55, v56, v57
	global_store_dwordx4 v[68:69], v[52:55], off
	s_nop 1
	v_mad_u64_u32 v[52:53], s[2:3], v148, s4, v[142:143]
	v_mov_b32_e32 v54, v53
	v_mad_u64_u32 v[54:55], s[2:3], v149, s4, v[54:55]
	v_mov_b32_e32 v53, v54
	v_mov_b32_e32 v54, v71
	v_pk_mul_f32 v[56:57], v[38:39], v[54:55] op_sel_hi:[1,0]
	v_pk_mul_f32 v[38:39], v[36:37], v[54:55] op_sel_hi:[1,0]
	v_pk_mul_f32 v[36:37], v[48:49], v[54:55] op_sel_hi:[1,0]
	v_pk_mul_f32 v[40:41], v[40:41], v[54:55] op_sel_hi:[1,0]
	v_pk_mul_f32 v[48:49], v[36:37], s[72:73]
	v_exp_f32_e32 v48, v48
	v_exp_f32_e32 v49, v49
	v_pk_mul_f32 v[50:51], v[50:51], v[54:55] op_sel_hi:[1,0]
	v_pk_mul_f32 v[42:43], v[42:43], v[54:55] op_sel_hi:[1,0]
	v_pk_add_f32 v[48:49], v[48:49], 1.0 op_sel_hi:[1,0]
	v_rcp_f32_e32 v48, v48
	v_rcp_f32_e32 v49, v49
	v_pk_mul_f32 v[44:45], v[44:45], v[54:55] op_sel_hi:[1,0]
	v_pk_mul_f32 v[46:47], v[46:47], v[54:55] op_sel_hi:[1,0]
	v_lshl_add_u64 v[52:53], v[52:53], 0, v[144:145]
	v_pk_mul_f32 v[36:37], v[36:37], v[48:49]
	s_nop 0
	v_pk_mul_f32 v[36:37], v[40:41], v[36:37]
	s_nop 0
	v_cvt_pk_bf16_f32 v36, v36, v37
	v_mul_f32_e32 v37, 0xbfb8aa3b, v50
	v_exp_f32_e32 v37, v37
	s_nop 0
	v_add_f32_e32 v37, 1.0, v37
	v_rcp_f32_e32 v40, v37
	v_mul_f32_e32 v37, 0xbfb8aa3b, v51
	v_exp_f32_e32 v37, v37
	s_nop 0
	v_add_f32_e32 v37, 1.0, v37
	v_rcp_f32_e32 v41, v37
	s_nop 0
	v_pk_mul_f32 v[40:41], v[50:51], v[40:41]
	s_nop 0
	v_pk_mul_f32 v[40:41], v[42:43], v[40:41]
	s_nop 0
	v_cvt_pk_bf16_f32 v37, v40, v41
	v_pk_mul_f32 v[40:41], v[44:45], s[72:73]
	v_exp_f32_e32 v40, v40
	v_exp_f32_e32 v41, v41
	s_nop 0
	v_pk_add_f32 v[40:41], v[40:41], 1.0 op_sel_hi:[1,0]
	v_rcp_f32_e32 v40, v40
	v_rcp_f32_e32 v41, v41
	s_nop 0
	v_pk_mul_f32 v[40:41], v[44:45], v[40:41]
	s_nop 0
	v_pk_mul_f32 v[38:39], v[38:39], v[40:41]
	s_nop 0
	v_cvt_pk_bf16_f32 v38, v38, v39
	v_mul_f32_e32 v39, 0xbfb8aa3b, v46
	v_exp_f32_e32 v39, v39
	s_nop 0
	v_add_f32_e32 v39, 1.0, v39
	v_rcp_f32_e32 v40, v39
	v_mul_f32_e32 v39, 0xbfb8aa3b, v47
	v_exp_f32_e32 v39, v39
	s_nop 0
	v_add_f32_e32 v39, 1.0, v39
	v_rcp_f32_e32 v41, v39
	s_nop 0
	v_pk_mul_f32 v[40:41], v[46:47], v[40:41]
	s_nop 0
	v_pk_mul_f32 v[40:41], v[56:57], v[40:41]
	s_nop 0
	v_cvt_pk_bf16_f32 v39, v40, v41
	global_store_dwordx4 v[52:53], v[36:39], off
	s_nop 1
	v_mad_u64_u32 v[36:37], s[2:3], v146, s4, v[142:143]
	v_mov_b32_e32 v38, v37
	v_mad_u64_u32 v[38:39], s[2:3], v147, s4, v[38:39]
	v_mov_b32_e32 v37, v38
	ds_read2_b32 v[38:39], v161 offset0:96 offset1:112
	v_lshl_add_u64 v[36:37], v[36:37], 0, v[144:145]
	s_waitcnt lgkmcnt(0)
; __device__ __forceinline__ unsigned cvt_pk_bf16(float lo, float hi) { f32x2_c v = {lo, hi}; bf16x2_c b = __builtin_convertvector(v, bf16x2_c); return __builtin_bit_cast(unsigned, b); }
; __device__ __forceinline__ float silu_f(float g) { return g * __builtin_amdgcn_rcpf(1.0f + __builtin_amdgcn_exp2f(-1.44269504f * g)); }
;     __device__ __forceinline__ void operator()(const f32x4 (&acc)[2][2][4][2], const Unit& u, int wr, int wc, int fr, int fq) const {
;     ...
;         for (int ai = 0; ai < 2; ++ai)
; #pragma unroll
;             for (int m = 0; m < 4; ++m) { bf16_t* rowp = O + (size_t)(row0 + ai * HALF + m * 16) * ldc + col0;
;                 const float rs = my[(ai * 4 + m) * 16];
;                 const f32x4 a0 = acc[ai][0][m][0] * rs, a1 = acc[ai][0][m][1] * rs, g0 = acc[ai][1][m][0] * rs, g1 = acc[ai][1][m][1] * rs;
;                 u32x4 w; w.x = cvt_pk_bf16(a0[0] * silu_f(g0[0]), a0[1] * silu_f(g0[1])); w.y = cvt_pk_bf16(a0[2] * silu_f(g0[2]), a0[3] * silu_f(g0[3]));
;                 w.z = cvt_pk_bf16(a1[0] * silu_f(g1[0]), a1[1] * silu_f(g1[1])); w.w = cvt_pk_bf16(a1[2] * silu_f(g1[2]), a1[3] * silu_f(g1[3]));
;                 *(u32x4*)rowp = w; }
	v_pk_mul_f32 v[40:41], v[22:23], v[38:39] op_sel_hi:[1,0]
	v_pk_mul_f32 v[22:23], v[20:21], v[38:39] op_sel_hi:[1,0]
	v_pk_mul_f32 v[20:21], v[32:33], v[38:39] op_sel_hi:[1,0]
	v_pk_mul_f32 v[24:25], v[24:25], v[38:39] op_sel_hi:[1,0]
	v_pk_mul_f32 v[32:33], v[20:21], s[72:73]
	v_exp_f32_e32 v32, v32
	v_exp_f32_e32 v33, v33
	v_pk_mul_f32 v[34:35], v[34:35], v[38:39] op_sel_hi:[1,0]
	v_pk_mul_f32 v[26:27], v[26:27], v[38:39] op_sel_hi:[1,0]
	v_pk_add_f32 v[32:33], v[32:33], 1.0 op_sel_hi:[1,0]
	v_rcp_f32_e32 v32, v32
	v_rcp_f32_e32 v33, v33
	v_pk_mul_f32 v[28:29], v[28:29], v[38:39] op_sel_hi:[1,0]
	v_pk_mul_f32 v[30:31], v[30:31], v[38:39] op_sel_hi:[1,0]
	v_pk_mul_f32 v[20:21], v[20:21], v[32:33]
	s_nop 0
	v_pk_mul_f32 v[20:21], v[24:25], v[20:21]
	s_nop 0
	v_cvt_pk_bf16_f32 v20, v20, v21
	v_mul_f32_e32 v21, 0xbfb8aa3b, v34
	v_exp_f32_e32 v21, v21
	s_nop 0
	v_add_f32_e32 v21, 1.0, v21
	v_rcp_f32_e32 v24, v21
	v_mul_f32_e32 v21, 0xbfb8aa3b, v35
	v_exp_f32_e32 v21, v21
	s_nop 0
	v_add_f32_e32 v21, 1.0, v21
	v_rcp_f32_e32 v25, v21
	s_nop 0
	v_pk_mul_f32 v[24:25], v[34:35], v[24:25]
	s_nop 0
	v_pk_mul_f32 v[24:25], v[26:27], v[24:25]
	s_nop 0
	v_cvt_pk_bf16_f32 v21, v24, v25
	v_pk_mul_f32 v[24:25], v[28:29], s[72:73]
	v_exp_f32_e32 v24, v24
	v_exp_f32_e32 v25, v25
	s_nop 0
	v_pk_add_f32 v[24:25], v[24:25], 1.0 op_sel_hi:[1,0]
	v_rcp_f32_e32 v24, v24
	v_rcp_f32_e32 v25, v25
	s_nop 0
	v_pk_mul_f32 v[24:25], v[28:29], v[24:25]
	s_nop 0
	v_pk_mul_f32 v[22:23], v[22:23], v[24:25]
	s_nop 0
	v_cvt_pk_bf16_f32 v22, v22, v23
	v_mul_f32_e32 v23, 0xbfb8aa3b, v30
	v_exp_f32_e32 v23, v23
	s_nop 0
	v_add_f32_e32 v23, 1.0, v23
	v_rcp_f32_e32 v24, v23
	v_mul_f32_e32 v23, 0xbfb8aa3b, v31
	v_exp_f32_e32 v23, v23
	s_nop 0
	v_add_f32_e32 v23, 1.0, v23
	v_rcp_f32_e32 v25, v23
	s_nop 0
	v_pk_mul_f32 v[24:25], v[30:31], v[24:25]
	s_nop 0
	v_pk_mul_f32 v[24:25], v[40:41], v[24:25]
	s_nop 0
	v_cvt_pk_bf16_f32 v23, v24, v25
	global_store_dwordx4 v[36:37], v[20:23], off
	s_nop 1
	v_mad_u64_u32 v[20:21], s[2:3], v140, s4, v[142:143]
	v_mov_b32_e32 v22, v21
	v_mad_u64_u32 v[22:23], s[2:3], v141, s4, v[22:23]
	v_mov_b32_e32 v21, v22
	v_mov_b32_e32 v22, v39
	v_pk_mul_f32 v[24:25], v[6:7], v[22:23] op_sel_hi:[1,0]
	v_pk_mul_f32 v[6:7], v[4:5], v[22:23] op_sel_hi:[1,0]
	v_pk_mul_f32 v[4:5], v[16:17], v[22:23] op_sel_hi:[1,0]
	v_pk_mul_f32 v[8:9], v[8:9], v[22:23] op_sel_hi:[1,0]
	v_pk_mul_f32 v[16:17], v[4:5], s[72:73]
	v_exp_f32_e32 v16, v16
	v_exp_f32_e32 v17, v17
	v_pk_mul_f32 v[18:19], v[18:19], v[22:23] op_sel_hi:[1,0]
	v_pk_mul_f32 v[10:11], v[10:11], v[22:23] op_sel_hi:[1,0]
	v_pk_add_f32 v[16:17], v[16:17], 1.0 op_sel_hi:[1,0]
	v_rcp_f32_e32 v16, v16
	v_rcp_f32_e32 v17, v17
	v_pk_mul_f32 v[12:13], v[12:13], v[22:23] op_sel_hi:[1,0]
	v_pk_mul_f32 v[14:15], v[14:15], v[22:23] op_sel_hi:[1,0]
	v_lshl_add_u64 v[20:21], v[20:21], 0, v[144:145]
	v_pk_mul_f32 v[4:5], v[4:5], v[16:17]
	s_mov_b64 s[4:5], -1
	v_pk_mul_f32 v[4:5], v[8:9], v[4:5]
	s_nop 0
	v_cvt_pk_bf16_f32 v4, v4, v5
	v_mul_f32_e32 v5, 0xbfb8aa3b, v18
	v_exp_f32_e32 v5, v5
	s_nop 0
	v_add_f32_e32 v5, 1.0, v5
	v_rcp_f32_e32 v8, v5
	v_mul_f32_e32 v5, 0xbfb8aa3b, v19
	v_exp_f32_e32 v5, v5
	s_nop 0
	v_add_f32_e32 v5, 1.0, v5
	v_rcp_f32_e32 v9, v5
	s_nop 0
	v_pk_mul_f32 v[8:9], v[18:19], v[8:9]
	s_nop 0
	v_pk_mul_f32 v[8:9], v[10:11], v[8:9]
	s_nop 0
	v_cvt_pk_bf16_f32 v5, v8, v9
	v_pk_mul_f32 v[8:9], v[12:13], s[72:73]
	v_exp_f32_e32 v8, v8
	v_exp_f32_e32 v9, v9
	s_nop 0
	v_pk_add_f32 v[8:9], v[8:9], 1.0 op_sel_hi:[1,0]
	v_rcp_f32_e32 v8, v8
	v_rcp_f32_e32 v9, v9
	s_nop 0
	v_pk_mul_f32 v[8:9], v[12:13], v[8:9]
	s_nop 0
	v_pk_mul_f32 v[6:7], v[6:7], v[8:9]
	s_nop 0
	v_cvt_pk_bf16_f32 v6, v6, v7
	v_mul_f32_e32 v7, 0xbfb8aa3b, v14
	v_exp_f32_e32 v7, v7
	s_nop 0
	v_add_f32_e32 v7, 1.0, v7
	v_rcp_f32_e32 v8, v7
	v_mul_f32_e32 v7, 0xbfb8aa3b, v15
	v_exp_f32_e32 v7, v7
	s_nop 0
	v_add_f32_e32 v7, 1.0, v7
	v_rcp_f32_e32 v9, v7
	s_nop 0
	v_pk_mul_f32 v[8:9], v[14:15], v[8:9]
	s_nop 0
	v_pk_mul_f32 v[8:9], v[24:25], v[8:9]
	s_nop 0
	v_cvt_pk_bf16_f32 v7, v8, v9
	global_store_dwordx4 v[20:21], v[4:7], off
	s_cbranch_vccnz .LBB0_124
	s_andn2_b64 vcc, exec, s[18:19]
	s_cbranch_vccnz .LBB0_123
	s_barrier
	s_branch .LBB0_123
